# BEST + dedicated conversion pass: loop back edge skips the loop-top vmcnt waits (they only serialised on the previous pair's non-temporal store acks)
# speedup vs baseline: 1.0107x; 1.0107x over previous
; __device__ __forceinline__ void p0_convert_fp8(const Params& P, LAS unsigned char* lds, int tid, int blk, int G, const int Lbeg, const int Lend) {
;     ...
;     for (;;) {
;         const int Ln = L + 2 * G; const bool moreA = Ln < Lend, moreB = (Ln + G) < Lend;
;         if (moreA) { cvt8_decode(P, Ln, nA); cvt8_load(nA, tid, qA); }
;         if (moreB) { cvt8_decode(P, Ln + G, nB); cvt8_load(nB, tid, qB); }
;     ...
;         if (!moreA) break;
;         uA = nA; uB = nB; hasB = moreB; L = Ln;
; #pragma unroll
;         for (int i = 0; i < 8; ++i) { rA[i] = qA[i]; rB[i] = qB[i]; }
.LBB0_301:
	s_andn2_b64 vcc, exec, s[6:7]
	s_cbranch_vccz .LBB0_219
	s_add_i32 s29, s58, s3
	v_mov_b64_e32 v[124:125], v[4:5]
	v_mov_b64_e32 v[120:121], v[8:9]
	v_mov_b64_e32 v[116:117], v[12:13]
	v_mov_b64_e32 v[112:113], v[16:17]
	v_mov_b64_e32 v[108:109], v[20:21]
	v_mov_b64_e32 v[104:105], v[24:25]
	v_mov_b64_e32 v[100:101], v[28:29]
	s_cmpk_lt_i32 s29, 0x2d00
	v_mov_b64_e32 v[128:129], v[36:37]
	s_mov_b64 s[46:47], s[30:31]
	s_mov_b64 s[34:35], s[4:5]
	s_mov_b32 s36, s49
	s_mov_b32 s61, s44
	s_mov_b32 s63, s28
	s_mov_b32 s37, s45
	s_mov_b32 s69, s50
	s_mov_b64 s[40:41], s[0:1]
	s_mov_b32 s42, s25
	s_mov_b32 s66, s8
	s_mov_b32 s68, s14
	s_mov_b32 s43, s9
	s_mov_b32 s72, s24
	v_mov_b64_e32 v[122:123], v[2:3]
	v_mov_b64_e32 v[118:119], v[6:7]
	v_mov_b64_e32 v[114:115], v[10:11]
	v_mov_b64_e32 v[110:111], v[14:15]
	v_mov_b64_e32 v[106:107], v[18:19]
	v_mov_b64_e32 v[102:103], v[22:23]
	v_mov_b64_e32 v[98:99], v[26:27]
	s_cselect_b64 s[38:39], -1, 0
	s_cmpk_gt_i32 s29, 0x2cff
	v_mov_b64_e32 v[126:127], v[34:35]
	s_branch .Lded_body

; __device__ __forceinline__ void cvt8_decode(const Params& P, int L, Cvt8Unit& u) {
;     if (L < 8192) { const int up = L >= 4096; const int r_ = L & 4095; const int e = r_ >> 7, r = r_ & 127;
;         u.src = P.in[up ? 24 : 23] + (size_t)e * 2048 * 1024; u.dst = P.ws + WS_WGU + (size_t)e * 2048 * 2048; u.Kd = 2048; u.Nd = 1024; u.k0 = (r >> 3) * 128; u.n0 = (r & 7) * 128; u.nmode = up ? 2 : 1; u.scale = WGU_SCALE; return; }
;     L -= 8192;
;     { const int e = L >> 7, r = L & 127; u.src = P.in[25] + (size_t)e * 1024 * 2048; u.dst = P.ws + WS_WD + (size_t)e * 2048 * 1024; u.Kd = 1024; u.Nd = 2048; u.k0 = (r >> 4) * 128; u.n0 = (r & 15) * 128; u.nmode = 0; u.scale = WD_SCALE; }
; __device__ __forceinline__ void p0_convert_fp8(const Params& P, LAS unsigned char* lds, int tid, int blk, int G, const int Lbeg, const int Lend) {
;     ...
;         const int Ln = L + 2 * G; const bool moreA = Ln < Lend, moreB = (Ln + G) < Lend;
;         if (moreA) { cvt8_decode(P, Ln, nA); cvt8_load(nA, tid, qA); }
;         if (moreB) { cvt8_decode(P, Ln + G, nB); cvt8_load(nB, tid, qB); }
.Lded_body:
	s_cbranch_scc1 .LBB0_309
	s_cmpk_gt_i32 s29, 0x1fff
	s_mov_b64 s[30:31], -1
	s_cbranch_scc0 .LBB0_305
	s_add_i32 s0, s29, 0xffffe000
	s_lshr_b32 s14, s0, 7
	s_lshl_b64 s[0:1], s[14:15], 23
	s_add_u32 s6, s18, s0
	s_addc_u32 s7, s19, s1
	s_lshl_b64 s[0:1], s[14:15], 21
	s_add_u32 s0, s53, s0
	s_addc_u32 s1, s54, s1
	s_add_i32 s8, s67, s57
	s_add_i32 s9, s77, s59
	s_and_b32 s8, s8, 0x380
	s_and_b32 s14, s9, 0x780
	s_mov_b64 s[30:31], 0
